# speedup vs baseline: 1.0475x; 1.0109x over previous
.LBB1_3:
	s_mov_b32 s29, s16
	v_add_u32_e32 v0, s29, v101
	ds_read_b128 v[94:97], v0 offset:16384
	ds_read_b128 v[102:105], v0 offset:17408
	ds_read_b128 v[106:109], v0 offset:18432
	ds_read_b128 v[110:113], v0 offset:19456
	ds_read_b128 v[114:117], v0 offset:32768
	ds_read_b128 v[118:121], v0 offset:33792
	ds_read_b128 v[122:125], v0 offset:34816
	ds_read_b128 v[126:129], v0 offset:35840
	v_add_u32_e32 v0, s29, v91
	ds_read_b128 v[130:133], v0
	ds_read_b128 v[134:137], v0 offset:1024
	ds_read_b128 v[138:141], v0 offset:2048
	ds_read_b128 v[142:145], v0 offset:3072
	ds_read_b128 v[146:149], v0 offset:4096
	ds_read_b128 v[150:153], v0 offset:5120
	ds_read_b128 v[154:157], v0 offset:6144
	ds_read_b128 v[158:161], v0 offset:7168
	s_lshl_b32 s16, s28, 2
	s_or_b32 s16, s16, s23
	s_lshl_b64 s[30:31], s[16:17], 19
	s_add_u32 s16, s6, s30
	s_addc_u32 s31, s7, s31
	s_lshl_b32 s33, s3, 7
	s_ashr_i32 s35, s33, 31
	s_add_u32 s30, s16, s33
	s_addc_u32 s31, s31, s35
	s_add_u32 s34, s4, s33
	s_addc_u32 s35, s5, s35
	s_add_i32 s16, s19, s27
	s_add_i32 m0, s16, 0x4000
	s_nop 0
	global_load_lds_dwordx4 v84, s[30:31]
	s_add_i32 m0, s16, 0x6000
	s_nop 0
	global_load_lds_dwordx4 v88, s[30:31]
	s_mov_b32 m0, s16
	s_nop 0
	global_load_lds_dwordx4 v82, s[34:35]
	s_waitcnt vmcnt(3)
	s_waitcnt lgkmcnt(0)
	s_barrier
	s_setprio 1
	s_waitcnt lgkmcnt(0)
	v_mfma_f32_16x16x32_f16 v[78:81], v[94:97], v[130:133], v[78:81]
	s_add_u32 s30, s30, 0x40000
	v_mfma_f32_16x16x32_f16 v[74:77], v[106:109], v[130:133], v[74:77]
	s_addc_u32 s31, s31, 0
	s_add_i32 m0, s16, 0x8000
	v_mfma_f32_16x16x32_f16 v[66:69], v[94:97], v[138:141], v[66:69]
	v_mfma_f32_16x16x32_f16 v[58:61], v[106:109], v[138:141], v[58:61]
	global_load_lds_dwordx4 v84, s[30:31]
	v_mfma_f32_16x16x32_f16 v[78:81], v[102:105], v[134:137], v[78:81]
	s_add_i32 m0, s16, 0xa000
	v_mfma_f32_16x16x32_f16 v[74:77], v[110:113], v[134:137], v[74:77]
	v_mfma_f32_16x16x32_f16 v[66:69], v[102:105], v[142:145], v[66:69]
	global_load_lds_dwordx4 v88, s[30:31]
	v_mfma_f32_16x16x32_f16 v[58:61], v[110:113], v[142:145], v[58:61]
	s_add_i32 m0, s16, 0x2000
	v_mfma_f32_16x16x32_f16 v[54:57], v[94:97], v[146:149], v[54:57]
	v_mfma_f32_16x16x32_f16 v[46:49], v[106:109], v[146:149], v[46:49]
	global_load_lds_dwordx4 v86, s[34:35]
	v_mfma_f32_16x16x32_f16 v[34:37], v[94:97], v[154:157], v[34:37]
	v_mfma_f32_16x16x32_f16 v[26:29], v[106:109], v[154:157], v[26:29]
	v_mfma_f32_16x16x32_f16 v[54:57], v[102:105], v[150:153], v[54:57]
	v_mfma_f32_16x16x32_f16 v[46:49], v[110:113], v[150:153], v[46:49]
	v_mfma_f32_16x16x32_f16 v[34:37], v[102:105], v[158:161], v[34:37]
	v_mfma_f32_16x16x32_f16 v[26:29], v[110:113], v[158:161], v[26:29]
	v_mfma_f32_16x16x32_f16 v[70:73], v[114:117], v[130:133], v[70:73]
	v_mfma_f32_16x16x32_f16 v[62:65], v[122:125], v[130:133], v[62:65]
	v_mfma_f32_16x16x32_f16 v[50:53], v[114:117], v[138:141], v[50:53]
	v_mfma_f32_16x16x32_f16 v[42:45], v[122:125], v[138:141], v[42:45]
	v_mfma_f32_16x16x32_f16 v[70:73], v[118:121], v[134:137], v[70:73]
	v_mfma_f32_16x16x32_f16 v[62:65], v[126:129], v[134:137], v[62:65]
	v_mfma_f32_16x16x32_f16 v[50:53], v[118:121], v[142:145], v[50:53]
	v_mfma_f32_16x16x32_f16 v[42:45], v[126:129], v[142:145], v[42:45]
	v_mfma_f32_16x16x32_f16 v[38:41], v[114:117], v[146:149], v[38:41]
	v_mfma_f32_16x16x32_f16 v[30:33], v[122:125], v[146:149], v[30:33]
	s_add_i32 s3, s3, 1
	s_cmp_lt_u32 s28, 2
	s_cselect_b64 s[30:31], -1, 0
	v_mfma_f32_16x16x32_f16 v[22:25], v[114:117], v[154:157], v[22:25]
	s_cmp_eq_u32 s3, 16
	s_cselect_b64 s[34:35], -1, 0
	v_mfma_f32_16x16x32_f16 v[2:5], v[122:125], v[154:157], v[2:5]
	s_and_b64 s[36:37], s[34:35], exec
	s_cselect_b32 s3, 0, s3
	v_mfma_f32_16x16x32_f16 v[38:41], v[118:121], v[150:153], v[38:41]
	s_and_b64 s[30:31], s[34:35], s[30:31]
	s_cmp_lg_u64 s[30:31], 0
	v_mfma_f32_16x16x32_f16 v[30:33], v[126:129], v[150:153], v[30:33]
	s_addc_u32 s28, s28, 0
	s_add_i32 s26, s26, -1
	v_mfma_f32_16x16x32_f16 v[22:25], v[118:121], v[158:161], v[22:25]
	s_mov_b32 s16, s24
	s_mov_b32 s24, s27
	v_mfma_f32_16x16x32_f16 v[2:5], v[126:129], v[158:161], v[2:5]
	s_mov_b32 s27, s29
	s_cmp_lg_u32 s26, 0
	s_setprio 0
	s_barrier
	s_cbranch_scc1 .LBB1_3
	s_lshl_b32 s3, s14, 7
	s_add_i32 s17, s25, s3
	s_ashr_i32 s3, s17, 1
	s_lshr_b32 s14, s17, 5
	s_or_b32 s24, s15, s2
	s_and_b32 s14, s14, 62
	s_and_b32 s27, s3, 0xfffffc00
	v_or_b32_e32 v105, s24, v1
	v_lshlrev_b32_e32 v98, 4, v93
	v_or_b32_e32 v102, 16, v93
	v_or_b32_e32 v103, 32, v93
	v_or_b32_e32 v104, 48, v93
	v_mov_b32_e32 v93, 0
	s_and_b32 s16, s24, 0x340
	v_lshlrev_b32_e32 v95, 6, v105
	s_or_b32 s2, s27, s14
	v_lshlrev_b32_e32 v0, 9, v92
	v_and_b32_e32 v110, 0xc00, v95
	v_mov_b32_e32 v111, v93
	s_or_b32 s14, s2, s16
	v_and_b32_e32 v92, 0x200, v0
	v_lshl_add_u64 v[110:111], s[8:9], 0, v[110:111]
	s_or_b32 s30, s14, 0x80
	s_mov_b32 s3, 0
	v_mov_b32_e32 v99, v93
	v_lshl_add_u64 v[110:111], v[110:111], 0, v[92:93]
	s_mov_b32 s2, 0x3e38aa3b
	v_pk_add_f32 v[72:73], v[12:13], v[72:73]
	v_pk_add_f32 v[70:71], v[10:11], v[70:71]
	v_pk_add_f32 v[64:65], v[8:9], v[64:65]
	v_pk_add_f32 v[62:63], v[6:7], v[62:63]
	s_ashr_i32 s31, s30, 31
	v_lshl_add_u64 v[112:113], v[110:111], 0, v[98:99]
	v_pk_mul_f32 v[72:73], v[72:73], s[2:3] op_sel_hi:[1,0]
	v_pk_mul_f32 v[70:71], v[70:71], s[2:3] op_sel_hi:[1,0]
	v_pk_mul_f32 v[64:65], v[64:65], s[2:3] op_sel_hi:[1,0]
	v_pk_mul_f32 v[62:63], v[62:63], s[2:3] op_sel_hi:[1,0]
	s_lshl_b64 s[30:31], s[30:31], 12
	v_lshlrev_b32_e32 v96, 4, v102
	v_mov_b32_e32 v97, v93
	v_pk_add_f32 v[80:81], v[20:21], v[80:81]
	v_pk_add_f32 v[78:79], v[18:19], v[78:79]
	v_pk_add_f32 v[74:75], v[14:15], v[74:75]
	s_ashr_i32 s15, s14, 31
	v_cvt_pk_f16_f32 v70, v70, v71
	v_cvt_pk_f16_f32 v71, v72, v73
	v_cvt_pk_f16_f32 v72, v62, v63
	v_cvt_pk_f16_f32 v73, v64, v65
	v_lshl_add_u64 v[62:63], v[112:113], 0, s[30:31]
	v_pk_add_f32 v[58:59], v[14:15], v[58:59]
	v_pk_mul_f32 v[80:81], v[80:81], s[2:3] op_sel_hi:[1,0]
	v_pk_mul_f32 v[78:79], v[78:79], s[2:3] op_sel_hi:[1,0]
	v_pk_mul_f32 v[74:75], v[74:75], s[2:3] op_sel_hi:[1,0]
	s_lshl_b64 s[28:29], s[14:15], 12
	global_store_dwordx4 v[62:63], v[70:73], off sc1
	v_pk_add_f32 v[62:63], v[20:21], v[68:69]
	v_pk_add_f32 v[64:65], v[18:19], v[66:67]
	v_lshl_add_u64 v[70:71], v[110:111], 0, v[96:97]
	v_pk_mul_f32 v[58:59], v[58:59], s[2:3] op_sel_hi:[1,0]
	v_pk_add_f32 v[52:53], v[12:13], v[52:53]
	v_pk_add_f32 v[50:51], v[10:11], v[50:51]
	v_pk_add_f32 v[44:45], v[8:9], v[44:45]
	v_pk_add_f32 v[42:43], v[6:7], v[42:43]
	v_lshlrev_b32_e32 v0, 4, v103
	v_cvt_pk_f16_f32 v78, v78, v79
	v_cvt_pk_f16_f32 v79, v80, v81
	v_cvt_pk_f16_f32 v80, v74, v75
	v_lshl_add_u64 v[74:75], v[112:113], 0, s[28:29]
	v_pk_mul_f32 v[66:67], v[62:63], s[2:3] op_sel_hi:[1,0]
	v_pk_mul_f32 v[62:63], v[64:65], s[2:3] op_sel_hi:[1,0]
	v_cvt_pk_f16_f32 v64, v58, v59
	v_lshl_add_u64 v[58:59], v[70:71], 0, s[28:29]
	v_pk_mul_f32 v[52:53], v[52:53], s[2:3] op_sel_hi:[1,0]
	v_pk_mul_f32 v[50:51], v[50:51], s[2:3] op_sel_hi:[1,0]
	v_pk_mul_f32 v[44:45], v[44:45], s[2:3] op_sel_hi:[1,0]
	v_pk_mul_f32 v[42:43], v[42:43], s[2:3] op_sel_hi:[1,0]
	s_or_b32 s28, s14, 1
	s_or_b32 s14, s14, 0x81
	v_and_b32_e32 v106, 0xf0, v0
	v_mov_b32_e32 v107, v93
	v_cvt_pk_f16_f32 v50, v50, v51
	v_cvt_pk_f16_f32 v51, v52, v53
	v_cvt_pk_f16_f32 v52, v42, v43
	v_cvt_pk_f16_f32 v53, v44, v45
	v_lshl_add_u64 v[42:43], v[70:71], 0, s[30:31]
	v_pk_add_f32 v[40:41], v[12:13], v[40:41]
	v_pk_add_f32 v[38:39], v[10:11], v[38:39]
	v_pk_add_f32 v[32:33], v[8:9], v[32:33]
	v_pk_add_f32 v[30:31], v[6:7], v[30:31]
	s_ashr_i32 s15, s14, 31
	v_lshlrev_b32_e32 v94, 4, v104
	global_store_dwordx4 v[42:43], v[50:53], off sc1
	v_pk_mul_f32 v[40:41], v[40:41], s[2:3] op_sel_hi:[1,0]
	v_pk_mul_f32 v[38:39], v[38:39], s[2:3] op_sel_hi:[1,0]
	v_lshl_add_u64 v[50:51], v[110:111], 0, v[106:107]
	v_pk_mul_f32 v[32:33], v[32:33], s[2:3] op_sel_hi:[1,0]
	v_pk_mul_f32 v[30:31], v[30:31], s[2:3] op_sel_hi:[1,0]
	s_lshl_b64 s[14:15], s[14:15], 12
	v_and_b32_e32 v108, 0x1f0, v94
	v_mov_b32_e32 v109, v93
	v_pk_add_f32 v[42:43], v[20:21], v[56:57]
	v_pk_add_f32 v[44:45], v[18:19], v[54:55]
	v_pk_add_f32 v[46:47], v[14:15], v[46:47]
	s_ashr_i32 s29, s28, 31
	v_cvt_pk_f16_f32 v38, v38, v39
	v_cvt_pk_f16_f32 v39, v40, v41
	v_cvt_pk_f16_f32 v40, v30, v31
	v_cvt_pk_f16_f32 v41, v32, v33
	v_lshl_add_u64 v[30:31], v[50:51], 0, s[14:15]
	v_pk_add_f32 v[20:21], v[20:21], v[36:37]
	v_pk_add_f32 v[18:19], v[18:19], v[34:35]
	v_pk_add_f32 v[14:15], v[14:15], v[26:27]
	v_pk_add_f32 v[76:77], v[16:17], v[76:77]
	v_pk_add_f32 v[60:61], v[16:17], v[60:61]
	v_pk_mul_f32 v[52:53], v[42:43], s[2:3] op_sel_hi:[1,0]
	v_pk_mul_f32 v[42:43], v[44:45], s[2:3] op_sel_hi:[1,0]
	v_pk_add_f32 v[44:45], v[16:17], v[48:49]
	s_lshl_b64 s[28:29], s[28:29], 12
	global_store_dwordx4 v[30:31], v[38:41], off sc1
	v_lshl_add_u64 v[30:31], v[110:111], 0, v[108:109]
	v_pk_mul_f32 v[20:21], v[20:21], s[2:3] op_sel_hi:[1,0]
	v_pk_mul_f32 v[18:19], v[18:19], s[2:3] op_sel_hi:[1,0]
	v_pk_add_f32 v[16:17], v[16:17], v[28:29]
	v_pk_mul_f32 v[14:15], v[14:15], s[2:3] op_sel_hi:[1,0]
	v_pk_add_f32 v[12:13], v[12:13], v[24:25]
	v_pk_add_f32 v[10:11], v[10:11], v[22:23]
	v_pk_add_f32 v[4:5], v[8:9], v[4:5]
	v_pk_add_f32 v[2:3], v[6:7], v[2:3]
	v_pk_mul_f32 v[76:77], v[76:77], s[2:3] op_sel_hi:[1,0]
	v_pk_mul_f32 v[60:61], v[60:61], s[2:3] op_sel_hi:[1,0]
	v_pk_mul_f32 v[48:49], v[44:45], s[2:3] op_sel_hi:[1,0]
	v_pk_mul_f32 v[44:45], v[46:47], s[2:3] op_sel_hi:[1,0]
	v_lshl_add_u64 v[46:47], v[50:51], 0, s[28:29]
	v_cvt_pk_f16_f32 v18, v18, v19
	v_cvt_pk_f16_f32 v19, v20, v21
	v_pk_mul_f32 v[16:17], v[16:17], s[2:3] op_sel_hi:[1,0]
	v_cvt_pk_f16_f32 v20, v14, v15
	v_lshl_add_u64 v[14:15], v[30:31], 0, s[28:29]
	v_pk_mul_f32 v[12:13], v[12:13], s[2:3] op_sel_hi:[1,0]
	v_pk_mul_f32 v[10:11], v[10:11], s[2:3] op_sel_hi:[1,0]
	v_pk_mul_f32 v[4:5], v[4:5], s[2:3] op_sel_hi:[1,0]
	v_pk_mul_f32 v[2:3], v[2:3], s[2:3] op_sel_hi:[1,0]
	s_add_u32 s28, s20, s22
	v_cvt_pk_f16_f32 v81, v76, v77
	v_cvt_pk_f16_f32 v62, v62, v63
	v_cvt_pk_f16_f32 v63, v66, v67
	v_cvt_pk_f16_f32 v65, v60, v61
	v_cvt_pk_f16_f32 v42, v42, v43
	v_cvt_pk_f16_f32 v43, v52, v53
	v_cvt_pk_f16_f32 v44, v44, v45
	v_cvt_pk_f16_f32 v45, v48, v49
	v_cvt_pk_f16_f32 v21, v16, v17
	v_cvt_pk_f16_f32 v10, v10, v11
	v_cvt_pk_f16_f32 v11, v12, v13
	v_cvt_pk_f16_f32 v12, v2, v3
	v_cvt_pk_f16_f32 v13, v4, v5
	v_lshl_add_u64 v[2:3], v[30:31], 0, s[14:15]
	s_addc_u32 s29, s21, 0
	v_lshlrev_b32_e32 v92, 2, v1
	global_store_dwordx4 v[74:75], v[78:81], off sc1
	global_store_dwordx4 v[58:59], v[62:65], off sc1
	global_store_dwordx4 v[46:47], v[42:45], off sc1
	global_store_dwordx4 v[14:15], v[18:21], off sc1
	global_store_dwordx4 v[2:3], v[10:13], off sc1
	v_lshl_add_u64 v[2:3], s[28:29], 0, v[92:93]
	s_mov_b64 s[28:29], 0x1000
	v_lshl_add_u64 v[10:11], v[2:3], 0, s[28:29]
	global_load_dwordx4 v[22:25], v[10:11], off
	global_load_dwordx4 v[14:17], v[10:11], off offset:16
	global_load_dwordx4 v[6:9], v[10:11], off offset:512
	global_load_dwordx4 v[2:5], v[10:11], off offset:528
	s_mov_b32 s25, 1
	s_mov_b32 s26, 16
	s_mov_b32 s14, 2
	s_mov_b32 s15, 0x18000
	s_mov_b32 s2, 0xc000
	s_mov_b32 s27, 0
	v_mov_b32_e32 v10, v93
	v_mov_b32_e32 v11, v93
	v_mov_b32_e32 v12, v93
	v_mov_b32_e32 v13, v93
	v_mov_b32_e32 v18, v93
	v_mov_b32_e32 v19, v93
	v_mov_b32_e32 v20, v93
	v_mov_b32_e32 v21, v93
	v_mov_b32_e32 v26, v93
	v_mov_b32_e32 v27, v93
	v_mov_b32_e32 v28, v93
	v_mov_b32_e32 v29, v93
	v_mov_b32_e32 v34, v93
	v_mov_b32_e32 v35, v93
	v_mov_b32_e32 v36, v93
	v_mov_b32_e32 v37, v93
	v_mov_b32_e32 v42, v93
	v_mov_b32_e32 v43, v93
	v_mov_b32_e32 v44, v93
	v_mov_b32_e32 v45, v93
	v_mov_b32_e32 v50, v93
	v_mov_b32_e32 v51, v93
	v_mov_b32_e32 v52, v93
	v_mov_b32_e32 v53, v93
	v_mov_b32_e32 v62, v93
	v_mov_b32_e32 v63, v93
	v_mov_b32_e32 v64, v93
	v_mov_b32_e32 v65, v93
	v_mov_b32_e32 v70, v93
	v_mov_b32_e32 v71, v93
	v_mov_b32_e32 v72, v93
	v_mov_b32_e32 v73, v93
	v_mov_b32_e32 v30, v93
	v_mov_b32_e32 v31, v93
	v_mov_b32_e32 v32, v93
	v_mov_b32_e32 v33, v93
	v_mov_b32_e32 v38, v93
	v_mov_b32_e32 v39, v93
	v_mov_b32_e32 v40, v93
	v_mov_b32_e32 v41, v93
	v_mov_b32_e32 v46, v93
	v_mov_b32_e32 v47, v93
	v_mov_b32_e32 v48, v93
	v_mov_b32_e32 v49, v93
	v_mov_b32_e32 v54, v93
	v_mov_b32_e32 v55, v93
	v_mov_b32_e32 v56, v93
	v_mov_b32_e32 v57, v93
	v_mov_b32_e32 v58, v93
	v_mov_b32_e32 v59, v93
	v_mov_b32_e32 v60, v93
	v_mov_b32_e32 v61, v93
	v_mov_b32_e32 v66, v93
	v_mov_b32_e32 v67, v93
	v_mov_b32_e32 v68, v93
	v_mov_b32_e32 v69, v93
	v_mov_b32_e32 v74, v93
	v_mov_b32_e32 v75, v93
	v_mov_b32_e32 v76, v93
	v_mov_b32_e32 v77, v93
	v_mov_b32_e32 v78, v93
	v_mov_b32_e32 v79, v93
	v_mov_b32_e32 v80, v93
	v_mov_b32_e32 v81, v93
.LBB1_5:
	s_mov_b32 s28, s2
	v_add_u32_e32 v1, s28, v101
	ds_read_b128 v[106:109], v1 offset:16384
	ds_read_b128 v[110:113], v1 offset:17408
	ds_read_b128 v[114:117], v1 offset:18432
	ds_read_b128 v[118:121], v1 offset:19456
	ds_read_b128 v[122:125], v1 offset:32768
	ds_read_b128 v[126:129], v1 offset:33792
	ds_read_b128 v[130:133], v1 offset:34816
	ds_read_b128 v[134:137], v1 offset:35840
	v_add_u32_e32 v1, s28, v91
	ds_read_b128 v[138:141], v1
	ds_read_b128 v[142:145], v1 offset:1024
	ds_read_b128 v[146:149], v1 offset:2048
	ds_read_b128 v[150:153], v1 offset:3072
	ds_read_b128 v[154:157], v1 offset:4096
	ds_read_b128 v[158:161], v1 offset:5120
	ds_read_b128 v[162:165], v1 offset:6144
	ds_read_b128 v[166:169], v1 offset:7168
	s_lshl_b32 s2, s25, 2
	s_or_b32 s2, s2, s23
	s_lshl_b64 s[30:31], s[2:3], 19
	s_add_u32 s2, s6, s30
	s_addc_u32 s29, s7, s31
	s_lshl_b32 s33, s14, 7
	s_ashr_i32 s35, s33, 31
	s_add_u32 s30, s2, s33
	s_addc_u32 s31, s29, s35
	s_add_u32 s34, s4, s33
	s_addc_u32 s35, s5, s35
	s_add_i32 s2, s19, s27
	s_add_i32 m0, s2, 0x4000
	s_nop 0
	global_load_lds_dwordx4 v84, s[30:31]
	s_add_i32 m0, s2, 0x6000
	s_nop 0
	global_load_lds_dwordx4 v88, s[30:31]
	s_mov_b32 m0, s2
	s_nop 0
	global_load_lds_dwordx4 v82, s[34:35]
	s_waitcnt vmcnt(3)
	s_waitcnt lgkmcnt(0)
	s_barrier
	s_setprio 1
	s_waitcnt lgkmcnt(0)
	v_mfma_f32_16x16x32_f16 v[78:81], v[106:109], v[138:141], v[78:81]
	s_add_u32 s30, s30, 0x40000
	v_mfma_f32_16x16x32_f16 v[74:77], v[114:117], v[138:141], v[74:77]
	s_addc_u32 s31, s31, 0
	s_add_i32 m0, s2, 0x8000
	v_mfma_f32_16x16x32_f16 v[66:69], v[106:109], v[146:149], v[66:69]
	v_mfma_f32_16x16x32_f16 v[58:61], v[114:117], v[146:149], v[58:61]
	global_load_lds_dwordx4 v84, s[30:31]
	v_mfma_f32_16x16x32_f16 v[78:81], v[110:113], v[142:145], v[78:81]
	s_add_i32 m0, s2, 0xa000
	v_mfma_f32_16x16x32_f16 v[74:77], v[118:121], v[142:145], v[74:77]
	v_mfma_f32_16x16x32_f16 v[66:69], v[110:113], v[150:153], v[66:69]
	global_load_lds_dwordx4 v88, s[30:31]
	v_mfma_f32_16x16x32_f16 v[58:61], v[118:121], v[150:153], v[58:61]
	s_add_i32 m0, s2, 0x2000
	v_mfma_f32_16x16x32_f16 v[54:57], v[106:109], v[154:157], v[54:57]
	v_mfma_f32_16x16x32_f16 v[46:49], v[114:117], v[154:157], v[46:49]
	global_load_lds_dwordx4 v86, s[34:35]
	v_mfma_f32_16x16x32_f16 v[38:41], v[106:109], v[162:165], v[38:41]
	v_mfma_f32_16x16x32_f16 v[30:33], v[114:117], v[162:165], v[30:33]
	v_mfma_f32_16x16x32_f16 v[54:57], v[110:113], v[158:161], v[54:57]
	v_mfma_f32_16x16x32_f16 v[46:49], v[118:121], v[158:161], v[46:49]
	v_mfma_f32_16x16x32_f16 v[38:41], v[110:113], v[166:169], v[38:41]
	v_mfma_f32_16x16x32_f16 v[30:33], v[118:121], v[166:169], v[30:33]
	v_mfma_f32_16x16x32_f16 v[70:73], v[122:125], v[138:141], v[70:73]
	v_mfma_f32_16x16x32_f16 v[62:65], v[130:133], v[138:141], v[62:65]
	v_mfma_f32_16x16x32_f16 v[50:53], v[122:125], v[146:149], v[50:53]
	v_mfma_f32_16x16x32_f16 v[42:45], v[130:133], v[146:149], v[42:45]
	v_mfma_f32_16x16x32_f16 v[70:73], v[126:129], v[142:145], v[70:73]
	v_mfma_f32_16x16x32_f16 v[62:65], v[134:137], v[142:145], v[62:65]
	v_mfma_f32_16x16x32_f16 v[50:53], v[126:129], v[150:153], v[50:53]
	v_mfma_f32_16x16x32_f16 v[42:45], v[134:137], v[150:153], v[42:45]
	v_mfma_f32_16x16x32_f16 v[34:37], v[122:125], v[154:157], v[34:37]
	v_mfma_f32_16x16x32_f16 v[26:29], v[130:133], v[154:157], v[26:29]
	s_add_i32 s2, s14, 1
	s_cmp_lt_u32 s25, 2
	s_cselect_b64 s[30:31], -1, 0
	v_mfma_f32_16x16x32_f16 v[18:21], v[122:125], v[162:165], v[18:21]
	s_cmp_eq_u32 s2, 16
	s_cselect_b64 s[34:35], -1, 0
	v_mfma_f32_16x16x32_f16 v[10:13], v[130:133], v[162:165], v[10:13]
	s_and_b64 s[36:37], s[34:35], exec
	s_cselect_b32 s14, 0, s2
	v_mfma_f32_16x16x32_f16 v[34:37], v[126:129], v[158:161], v[34:37]
	s_and_b64 s[30:31], s[34:35], s[30:31]
	s_cmp_lg_u64 s[30:31], 0
	v_mfma_f32_16x16x32_f16 v[26:29], v[134:137], v[158:161], v[26:29]
	s_addc_u32 s25, s25, 0
	s_add_i32 s26, s26, -1
	v_mfma_f32_16x16x32_f16 v[18:21], v[126:129], v[166:169], v[18:21]
	s_mov_b32 s2, s15
	s_mov_b32 s15, s27
	v_mfma_f32_16x16x32_f16 v[10:13], v[134:137], v[166:169], v[10:13]
	s_mov_b32 s27, s28
	s_cmp_lg_u32 s26, 0
	s_setprio 0
	s_barrier
	s_cbranch_scc1 .LBB1_5
	s_ashr_i32 s2, s17, 7
	s_and_b32 s3, s2, -16
	s_or_b32 s2, s3, 2
	s_sub_u32 s14, s10, s8
	s_subb_u32 s11, s11, s9
	s_bfe_u32 s6, s17, 0x50006
	s_add_u32 s14, s8, s14
	s_addc_u32 s15, s9, s11
	s_lshr_b32 s11, s24, 6
	s_or_b32 s17, s11, s3
	s_lshl_b32 s17, s17, 8
	s_lshl_b32 s23, s6, 3
	v_bfe_u32 v93, v105, 3, 3
	v_pk_add_f32 v[80:81], v[24:25], v[80:81]
	v_pk_add_f32 v[78:79], v[22:23], v[78:79]
	v_pk_add_f32 v[74:75], v[14:15], v[74:75]
	s_or_b32 s17, s17, s23
	s_or_b32 s11, s2, s11
	v_cvt_pk_f16_f32 v78, v78, v79
	v_cvt_pk_f16_f32 v79, v80, v81
	v_cvt_pk_f16_f32 v80, v74, v75
	v_or_b32_e32 v74, s17, v93
	s_lshl_b32 s11, s11, 8
	v_ashrrev_i32_e32 v75, 31, v74
	v_pk_add_f32 v[72:73], v[8:9], v[72:73]
	v_pk_add_f32 v[70:71], v[6:7], v[70:71]
	v_pk_add_f32 v[62:63], v[2:3], v[62:63]
	s_or_b32 s11, s11, s23
	v_lshlrev_b64 v[74:75], 10, v[74:75]
	v_cvt_pk_f16_f32 v70, v70, v71
	v_cvt_pk_f16_f32 v71, v72, v73
	v_cvt_pk_f16_f32 v72, v62, v63
	v_or_b32_e32 v62, s11, v93
	v_pk_add_f32 v[76:77], v[16:17], v[76:77]
	v_lshl_add_u64 v[74:75], s[14:15], 0, v[74:75]
	v_ashrrev_i32_e32 v63, 31, v62
	v_cvt_pk_f16_f32 v81, v76, v77
	v_lshl_add_u64 v[76:77], v[74:75], 0, v[98:99]
	v_lshlrev_b64 v[62:63], 10, v[62:63]
	global_store_dwordx4 v[76:77], v[78:81], off sc1
	v_pk_add_f32 v[64:65], v[4:5], v[64:65]
	v_lshl_add_u64 v[76:77], s[14:15], 0, v[62:63]
	v_cvt_pk_f16_f32 v73, v64, v65
	v_lshl_add_u64 v[62:63], v[76:77], 0, v[98:99]
	global_store_dwordx4 v[62:63], v[70:73], off sc1
	v_pk_add_f32 v[64:65], v[24:25], v[68:69]
	v_pk_add_f32 v[62:63], v[22:23], v[66:67]
	v_pk_add_f32 v[60:61], v[16:17], v[60:61]
	v_pk_add_f32 v[58:59], v[14:15], v[58:59]
	v_pk_add_f32 v[52:53], v[8:9], v[52:53]
	v_pk_add_f32 v[50:51], v[6:7], v[50:51]
	v_pk_add_f32 v[44:45], v[4:5], v[44:45]
	v_pk_add_f32 v[42:43], v[2:3], v[42:43]
	v_cvt_pk_f16_f32 v62, v62, v63
	v_cvt_pk_f16_f32 v63, v64, v65
	v_cvt_pk_f16_f32 v64, v58, v59
	v_cvt_pk_f16_f32 v65, v60, v61
	v_lshl_add_u64 v[58:59], v[74:75], 0, v[96:97]
	v_cvt_pk_f16_f32 v50, v50, v51
	v_cvt_pk_f16_f32 v51, v52, v53
	v_cvt_pk_f16_f32 v52, v42, v43
	v_cvt_pk_f16_f32 v53, v44, v45
	v_lshl_add_u64 v[42:43], v[76:77], 0, v[96:97]
	v_mov_b32_e32 v1, 0
	global_store_dwordx4 v[58:59], v[62:65], off sc1
	global_store_dwordx4 v[42:43], v[50:53], off sc1
	v_pk_add_f32 v[44:45], v[24:25], v[56:57]
	v_pk_add_f32 v[42:43], v[22:23], v[54:55]
	v_mov_b32_e32 v95, v1
	v_cvt_pk_f16_f32 v42, v42, v43
	v_cvt_pk_f16_f32 v43, v44, v45
	v_pk_add_f32 v[48:49], v[16:17], v[48:49]
	v_pk_add_f32 v[44:45], v[14:15], v[46:47]
	v_pk_add_f32 v[36:37], v[8:9], v[36:37]
	v_pk_add_f32 v[34:35], v[6:7], v[34:35]
	v_pk_add_f32 v[28:29], v[4:5], v[28:29]
	v_pk_add_f32 v[26:27], v[2:3], v[26:27]
	v_pk_add_f32 v[24:25], v[24:25], v[40:41]
	v_pk_add_f32 v[22:23], v[22:23], v[38:39]
	v_pk_add_f32 v[16:17], v[16:17], v[32:33]
	v_pk_add_f32 v[14:15], v[14:15], v[30:31]
	v_pk_add_f32 v[8:9], v[8:9], v[20:21]
	v_pk_add_f32 v[6:7], v[6:7], v[18:19]
	v_pk_add_f32 v[4:5], v[4:5], v[12:13]
	v_pk_add_f32 v[2:3], v[2:3], v[10:11]
	s_add_u32 s14, s20, s22
	v_cvt_pk_f16_f32 v44, v44, v45
	v_cvt_pk_f16_f32 v45, v48, v49
	v_lshl_add_u64 v[46:47], v[74:75], 0, v[0:1]
	v_cvt_pk_f16_f32 v34, v34, v35
	v_cvt_pk_f16_f32 v35, v36, v37
	v_cvt_pk_f16_f32 v36, v26, v27
	v_cvt_pk_f16_f32 v37, v28, v29
	v_lshl_add_u64 v[26:27], v[76:77], 0, v[0:1]
	v_cvt_pk_f16_f32 v22, v22, v23
	v_cvt_pk_f16_f32 v23, v24, v25
	v_cvt_pk_f16_f32 v24, v14, v15
	v_cvt_pk_f16_f32 v25, v16, v17
	v_lshl_add_u64 v[14:15], v[74:75], 0, v[94:95]
	v_cvt_pk_f16_f32 v6, v6, v7
	v_cvt_pk_f16_f32 v7, v8, v9
	v_cvt_pk_f16_f32 v8, v2, v3
	v_cvt_pk_f16_f32 v9, v4, v5
	v_lshl_add_u64 v[2:3], v[76:77], 0, v[94:95]
	s_addc_u32 s15, s21, 0
	v_mov_b32_e32 v93, v1
	global_store_dwordx4 v[46:47], v[42:45], off sc1
	global_store_dwordx4 v[26:27], v[34:37], off sc1
	global_store_dwordx4 v[14:15], v[22:25], off sc1
	global_store_dwordx4 v[2:3], v[6:9], off sc1
	v_lshl_add_u64 v[2:3], s[14:15], 0, v[92:93]
	s_mov_b64 s[14:15], 0x2000
	v_lshl_add_u64 v[2:3], v[2:3], 0, s[14:15]
	global_load_dwordx4 v[20:23], v[2:3], off
	global_load_dwordx4 v[12:15], v[2:3], off offset:16
	global_load_dwordx4 v[8:11], v[2:3], off offset:512
	global_load_dwordx4 v[4:7], v[2:3], off offset:528
	s_add_u32 s11, s12, 0x400000
	s_mov_b32 s7, 2
	v_and_b32_e32 v106, 56, v105
	s_mov_b32 s10, 0
	s_addc_u32 s12, s13, 0
	s_mov_b32 s14, 0xc000
	s_mov_b32 s17, 0x18000
	s_mov_b32 s13, 16
	v_mov_b32_e32 v0, v1
	v_mov_b32_e32 v2, v1
	v_mov_b32_e32 v3, v1
	v_mov_b32_e32 v16, v1
	v_mov_b32_e32 v17, v1
	v_mov_b32_e32 v18, v1
	v_mov_b32_e32 v19, v1
	v_mov_b32_e32 v24, v1
	v_mov_b32_e32 v25, v1
	v_mov_b32_e32 v26, v1
	v_mov_b32_e32 v27, v1
	v_mov_b32_e32 v32, v1
	v_mov_b32_e32 v33, v1
	v_mov_b32_e32 v34, v1
	v_mov_b32_e32 v35, v1
	v_mov_b32_e32 v40, v1
	v_mov_b32_e32 v41, v1
	v_mov_b32_e32 v42, v1
	v_mov_b32_e32 v43, v1
	v_mov_b32_e32 v48, v1
	v_mov_b32_e32 v49, v1
	v_mov_b32_e32 v50, v1
	v_mov_b32_e32 v51, v1
	v_mov_b32_e32 v60, v1
	v_mov_b32_e32 v61, v1
	v_mov_b32_e32 v62, v1
	v_mov_b32_e32 v63, v1
	v_mov_b32_e32 v68, v1
	v_mov_b32_e32 v69, v1
	v_mov_b32_e32 v70, v1
	v_mov_b32_e32 v71, v1
	v_mov_b32_e32 v28, v1
	v_mov_b32_e32 v29, v1
	v_mov_b32_e32 v30, v1
	v_mov_b32_e32 v31, v1
	v_mov_b32_e32 v36, v1
	v_mov_b32_e32 v37, v1
	v_mov_b32_e32 v38, v1
	v_mov_b32_e32 v39, v1
	v_mov_b32_e32 v44, v1
	v_mov_b32_e32 v45, v1
	v_mov_b32_e32 v46, v1
	v_mov_b32_e32 v47, v1
	v_mov_b32_e32 v52, v1
	v_mov_b32_e32 v53, v1
	v_mov_b32_e32 v54, v1
	v_mov_b32_e32 v55, v1
	v_mov_b32_e32 v56, v1
	v_mov_b32_e32 v57, v1
	v_mov_b32_e32 v58, v1
	v_mov_b32_e32 v59, v1
	v_mov_b32_e32 v64, v1
	v_mov_b32_e32 v65, v1
	v_mov_b32_e32 v66, v1
	v_mov_b32_e32 v67, v1
	v_mov_b32_e32 v72, v1
	v_mov_b32_e32 v73, v1
	v_mov_b32_e32 v74, v1
	v_mov_b32_e32 v75, v1
	v_mov_b32_e32 v76, v1
	v_mov_b32_e32 v77, v1
	v_mov_b32_e32 v78, v1
	v_mov_b32_e32 v79, v1
.LBB1_7:
	s_mov_b32 s15, s17
	v_add_u32_e32 v80, s15, v101
	ds_read_b128 v[92:95], v80 offset:16384
	ds_read_b128 v[96:99], v80 offset:17408
	ds_read_b128 v[108:111], v80 offset:18432
	ds_read_b128 v[112:115], v80 offset:19456
	ds_read_b128 v[116:119], v80 offset:32768
	ds_read_b128 v[120:123], v80 offset:33792
	ds_read_b128 v[124:127], v80 offset:34816
	ds_read_b128 v[128:131], v80 offset:35840
	v_add_u32_e32 v80, s15, v91
	ds_read_b128 v[132:135], v80
	ds_read_b128 v[136:139], v80 offset:1024
	ds_read_b128 v[140:143], v80 offset:2048
	ds_read_b128 v[144:147], v80 offset:3072
	ds_read_b128 v[148:151], v80 offset:4096
	ds_read_b128 v[152:155], v80 offset:5120
	ds_read_b128 v[156:159], v80 offset:6144
	ds_read_b128 v[160:163], v80 offset:7168
	s_lshl_b32 s17, s7, 7
	s_ashr_i32 s23, s17, 31
	s_add_u32 s20, s11, s17
	s_addc_u32 s21, s12, s23
	s_add_u32 s22, s4, s17
	s_addc_u32 s23, s5, s23
	s_add_i32 s17, s19, s14
	s_add_i32 m0, s17, 0x4000
	s_nop 0
	global_load_lds_dwordx4 v84, s[20:21]
	s_add_i32 m0, s17, 0x6000
	s_nop 0
	global_load_lds_dwordx4 v88, s[20:21]
	s_mov_b32 m0, s17
	s_nop 0
	global_load_lds_dwordx4 v82, s[22:23]
	s_waitcnt vmcnt(3)
	s_waitcnt lgkmcnt(0)
	s_barrier
	s_setprio 1
	s_waitcnt lgkmcnt(0)
	v_mfma_f32_16x16x32_f16 v[76:79], v[92:95], v[132:135], v[76:79]
	s_add_u32 s20, s20, 0x40000
	v_mfma_f32_16x16x32_f16 v[72:75], v[108:111], v[132:135], v[72:75]
	s_addc_u32 s21, s21, 0
	s_add_i32 m0, s17, 0x8000
	v_mfma_f32_16x16x32_f16 v[64:67], v[92:95], v[140:143], v[64:67]
	v_mfma_f32_16x16x32_f16 v[56:59], v[108:111], v[140:143], v[56:59]
	global_load_lds_dwordx4 v84, s[20:21]
	v_mfma_f32_16x16x32_f16 v[76:79], v[96:99], v[136:139], v[76:79]
	s_add_i32 m0, s17, 0xa000
	v_mfma_f32_16x16x32_f16 v[72:75], v[112:115], v[136:139], v[72:75]
	v_mfma_f32_16x16x32_f16 v[64:67], v[96:99], v[144:147], v[64:67]
	global_load_lds_dwordx4 v88, s[20:21]
	v_mfma_f32_16x16x32_f16 v[56:59], v[112:115], v[144:147], v[56:59]
	s_add_i32 m0, s17, 0x2000
	v_mfma_f32_16x16x32_f16 v[52:55], v[92:95], v[148:151], v[52:55]
	v_mfma_f32_16x16x32_f16 v[44:47], v[108:111], v[148:151], v[44:47]
	global_load_lds_dwordx4 v86, s[22:23]
	v_mfma_f32_16x16x32_f16 v[36:39], v[92:95], v[156:159], v[36:39]
	v_mfma_f32_16x16x32_f16 v[28:31], v[108:111], v[156:159], v[28:31]
	v_mfma_f32_16x16x32_f16 v[52:55], v[96:99], v[152:155], v[52:55]
	v_mfma_f32_16x16x32_f16 v[44:47], v[112:115], v[152:155], v[44:47]
	v_mfma_f32_16x16x32_f16 v[36:39], v[96:99], v[160:163], v[36:39]
	v_mfma_f32_16x16x32_f16 v[28:31], v[112:115], v[160:163], v[28:31]
	v_mfma_f32_16x16x32_f16 v[68:71], v[116:119], v[132:135], v[68:71]
	v_mfma_f32_16x16x32_f16 v[60:63], v[124:127], v[132:135], v[60:63]
	v_mfma_f32_16x16x32_f16 v[48:51], v[116:119], v[140:143], v[48:51]
	v_mfma_f32_16x16x32_f16 v[40:43], v[124:127], v[140:143], v[40:43]
	v_mfma_f32_16x16x32_f16 v[68:71], v[120:123], v[136:139], v[68:71]
	v_mfma_f32_16x16x32_f16 v[60:63], v[128:131], v[136:139], v[60:63]
	v_mfma_f32_16x16x32_f16 v[48:51], v[120:123], v[144:147], v[48:51]
	v_mfma_f32_16x16x32_f16 v[40:43], v[128:131], v[144:147], v[40:43]
	v_mfma_f32_16x16x32_f16 v[32:35], v[116:119], v[148:151], v[32:35]
	v_mfma_f32_16x16x32_f16 v[24:27], v[124:127], v[148:151], v[24:27]
	s_add_i32 s7, s7, 1
	s_cmp_lg_u32 s7, 16
	v_mfma_f32_16x16x32_f16 v[16:19], v[116:119], v[156:159], v[16:19]
	s_cselect_b32 s7, s7, 0
	v_mfma_f32_16x16x32_f16 v[0:3], v[124:127], v[156:159], v[0:3]
	s_add_i32 s13, s13, -1
	v_mfma_f32_16x16x32_f16 v[32:35], v[120:123], v[152:155], v[32:35]
	s_mov_b32 s17, s10
	v_mfma_f32_16x16x32_f16 v[24:27], v[128:131], v[152:155], v[24:27]
	s_mov_b32 s10, s14
	v_mfma_f32_16x16x32_f16 v[16:19], v[120:123], v[160:163], v[16:19]
	s_mov_b32 s14, s15
	v_mfma_f32_16x16x32_f16 v[0:3], v[128:131], v[160:163], v[0:3]
	s_cmp_lg_u32 s13, 0
	s_setprio 0
	s_barrier
	s_cbranch_scc1 .LBB1_7
	s_sub_u32 s0, s0, s8
	s_subb_u32 s1, s1, s9
	s_add_u32 s0, s8, s0
	s_addc_u32 s1, s9, s1
	s_lshl_b32 s3, s3, 6
	s_or_b32 s3, s3, s16
	s_lshl_b32 s4, s6, 1
	v_lshrrev_b32_e32 v86, 5, v106
	v_pk_add_f32 v[78:79], v[22:23], v[78:79]
	v_pk_add_f32 v[76:77], v[20:21], v[76:77]
	v_pk_add_f32 v[72:73], v[12:13], v[72:73]
	s_or_b32 s3, s3, s4
	s_lshl_b32 s2, s2, 6
	v_cvt_pk_f16_f32 v76, v76, v77
	v_cvt_pk_f16_f32 v77, v78, v79
	v_cvt_pk_f16_f32 v78, v72, v73
	v_or_b32_e32 v72, s3, v86
	s_or_b32 s2, s2, s16
	v_ashrrev_i32_e32 v73, 31, v72
	v_pk_add_f32 v[70:71], v[10:11], v[70:71]
	v_pk_add_f32 v[68:69], v[8:9], v[68:69]
	v_pk_add_f32 v[60:61], v[4:5], v[60:61]
	s_or_b32 s2, s2, s4
	v_lshlrev_b64 v[72:73], 12, v[72:73]
	v_cvt_pk_f16_f32 v68, v68, v69
	v_cvt_pk_f16_f32 v69, v70, v71
	v_cvt_pk_f16_f32 v70, v60, v61
	v_or_b32_e32 v60, s2, v86
	v_mov_b32_e32 v91, 0
	v_pk_add_f32 v[74:75], v[14:15], v[74:75]
	v_lshl_add_u64 v[72:73], s[0:1], 0, v[72:73]
	v_ashrrev_i32_e32 v61, 31, v60
	v_cvt_pk_f16_f32 v79, v74, v75
	v_lshl_add_u64 v[74:75], v[72:73], 0, v[90:91]
	v_lshlrev_b64 v[60:61], 12, v[60:61]
	v_lshl_or_b32 v84, v102, 6, v100
	v_mov_b32_e32 v85, v91
	global_store_dwordx4 v[74:75], v[76:79], off sc1
	v_lshl_add_u64 v[74:75], s[0:1], 0, v[60:61]
	v_pk_add_f32 v[50:51], v[10:11], v[50:51]
	v_pk_add_f32 v[48:49], v[8:9], v[48:49]
	v_pk_add_f32 v[42:43], v[6:7], v[42:43]
	v_pk_add_f32 v[40:41], v[4:5], v[40:41]
	v_pk_add_f32 v[62:63], v[6:7], v[62:63]
	v_cvt_pk_f16_f32 v48, v48, v49
	v_cvt_pk_f16_f32 v49, v50, v51
	v_cvt_pk_f16_f32 v50, v40, v41
	v_cvt_pk_f16_f32 v51, v42, v43
	v_lshl_add_u64 v[40:41], v[74:75], 0, v[84:85]
	v_cvt_pk_f16_f32 v71, v62, v63
	v_lshl_add_u64 v[60:61], v[74:75], 0, v[90:91]
	global_store_dwordx4 v[40:41], v[48:51], off sc1
	v_pk_add_f32 v[42:43], v[22:23], v[54:55]
	v_pk_add_f32 v[40:41], v[20:21], v[52:53]
	v_lshl_or_b32 v80, v103, 6, v100
	v_lshl_or_b32 v82, v104, 6, v100
	v_mov_b32_e32 v81, v91
	v_mov_b32_e32 v83, v91
	global_store_dwordx4 v[60:61], v[68:71], off sc1
	v_pk_add_f32 v[62:63], v[22:23], v[66:67]
	v_pk_add_f32 v[60:61], v[20:21], v[64:65]
	v_pk_add_f32 v[58:59], v[14:15], v[58:59]
	v_pk_add_f32 v[56:57], v[12:13], v[56:57]
	v_cvt_pk_f16_f32 v40, v40, v41
	v_cvt_pk_f16_f32 v41, v42, v43
	v_pk_add_f32 v[46:47], v[14:15], v[46:47]
	v_pk_add_f32 v[42:43], v[12:13], v[44:45]
	v_pk_add_f32 v[34:35], v[10:11], v[34:35]
	v_pk_add_f32 v[32:33], v[8:9], v[32:33]
	v_pk_add_f32 v[26:27], v[6:7], v[26:27]
	v_pk_add_f32 v[24:25], v[4:5], v[24:25]
	v_pk_add_f32 v[22:23], v[22:23], v[38:39]
	v_pk_add_f32 v[20:21], v[20:21], v[36:37]
	v_pk_add_f32 v[14:15], v[14:15], v[30:31]
	v_pk_add_f32 v[12:13], v[12:13], v[28:29]
	v_pk_add_f32 v[10:11], v[10:11], v[18:19]
	v_pk_add_f32 v[8:9], v[8:9], v[16:17]
	v_pk_add_f32 v[2:3], v[6:7], v[2:3]
	v_pk_add_f32 v[0:1], v[4:5], v[0:1]
	v_cvt_pk_f16_f32 v60, v60, v61
	v_cvt_pk_f16_f32 v61, v62, v63
	v_cvt_pk_f16_f32 v62, v56, v57
	v_cvt_pk_f16_f32 v63, v58, v59
	v_lshl_add_u64 v[56:57], v[72:73], 0, v[84:85]
	v_cvt_pk_f16_f32 v42, v42, v43
	v_cvt_pk_f16_f32 v43, v46, v47
	v_lshl_add_u64 v[44:45], v[72:73], 0, v[80:81]
	v_cvt_pk_f16_f32 v32, v32, v33
	v_cvt_pk_f16_f32 v33, v34, v35
	v_cvt_pk_f16_f32 v34, v24, v25
	v_cvt_pk_f16_f32 v35, v26, v27
	v_lshl_add_u64 v[24:25], v[74:75], 0, v[80:81]
	v_cvt_pk_f16_f32 v20, v20, v21
	v_cvt_pk_f16_f32 v21, v22, v23
	v_cvt_pk_f16_f32 v22, v12, v13
	v_cvt_pk_f16_f32 v23, v14, v15
	v_lshl_add_u64 v[12:13], v[72:73], 0, v[82:83]
	v_cvt_pk_f16_f32 v8, v8, v9
	v_cvt_pk_f16_f32 v9, v10, v11
	v_cvt_pk_f16_f32 v10, v0, v1
	v_cvt_pk_f16_f32 v11, v2, v3
	v_lshl_add_u64 v[0:1], v[74:75], 0, v[82:83]
	global_store_dwordx4 v[56:57], v[60:63], off sc1
	global_store_dwordx4 v[44:45], v[40:43], off sc1
	global_store_dwordx4 v[24:25], v[32:35], off sc1
	global_store_dwordx4 v[12:13], v[20:23], off sc1
	global_store_dwordx4 v[0:1], v[8:11], off sc1
	s_waitcnt vmcnt(0)
	s_cmpk_gt_u32 s18, 0xff
	s_cbranch_scc1 .LBB1_10
	s_barrier

.LBB2_3:
	s_mov_b32 s16, s15
	v_add_u32_e32 v116, s16, v87
	v_add_u32_e32 v148, s16, v0
	ds_read_b128 v[88:91], v116 offset:16384
	ds_read_b128 v[92:95], v116 offset:17408
	ds_read_b128 v[96:99], v116 offset:18432
	ds_read_b128 v[100:103], v116 offset:19456
	ds_read_b128 v[104:107], v116 offset:32768
	ds_read_b128 v[108:111], v116 offset:33792
	ds_read_b128 v[112:115], v116 offset:34816
	ds_read_b128 v[116:119], v116 offset:35840
	ds_read_b128 v[120:123], v148
	ds_read_b128 v[124:127], v148 offset:1024
	ds_read_b128 v[128:131], v148 offset:2048
	ds_read_b128 v[132:135], v148 offset:3072
	ds_read_b128 v[136:139], v148 offset:4096
	ds_read_b128 v[140:143], v148 offset:5120
	ds_read_b128 v[144:147], v148 offset:6144
	ds_read_b128 v[148:151], v148 offset:7168
	s_lshl_b32 s15, s7, 7
	s_ashr_i32 s17, s15, 31
	s_add_u32 s18, s4, s15
	s_addc_u32 s19, s5, s17
	s_add_u32 s20, s2, s15
	s_addc_u32 s21, s3, s17
	s_add_i32 s15, s6, s14
	s_add_i32 m0, s15, 0x4000
	s_nop 0
	global_load_lds_dwordx4 v82, s[18:19]
	s_add_i32 m0, s15, 0x6000
	s_nop 0
	global_load_lds_dwordx4 v84, s[18:19]
	s_mov_b32 m0, s15
	s_nop 0
	global_load_lds_dwordx4 v82, s[20:21]
	s_waitcnt vmcnt(3)
	s_waitcnt lgkmcnt(0)
	s_barrier
	s_setprio 1
	s_waitcnt lgkmcnt(0)
	v_mfma_f32_16x16x32_f16 v[18:21], v[88:91], v[120:123], v[18:21]
	s_add_u32 s18, s18, 0x40000
	v_mfma_f32_16x16x32_f16 v[70:73], v[96:99], v[120:123], v[70:73]
	s_addc_u32 s19, s19, 0
	s_add_i32 m0, s15, 0x8000
	v_mfma_f32_16x16x32_f16 v[58:61], v[88:91], v[128:131], v[58:61]
	v_mfma_f32_16x16x32_f16 v[54:57], v[96:99], v[128:131], v[54:57]
	global_load_lds_dwordx4 v82, s[18:19]
	v_mfma_f32_16x16x32_f16 v[18:21], v[92:95], v[124:127], v[18:21]
	s_add_i32 m0, s15, 0xa000
	v_mfma_f32_16x16x32_f16 v[70:73], v[100:103], v[124:127], v[70:73]
	v_mfma_f32_16x16x32_f16 v[58:61], v[92:95], v[132:135], v[58:61]
	global_load_lds_dwordx4 v84, s[18:19]
	v_mfma_f32_16x16x32_f16 v[54:57], v[100:103], v[132:135], v[54:57]
	s_add_i32 m0, s15, 0x2000
	v_mfma_f32_16x16x32_f16 v[42:45], v[88:91], v[136:139], v[42:45]
	v_mfma_f32_16x16x32_f16 v[38:41], v[96:99], v[136:139], v[38:41]
	global_load_lds_dwordx4 v84, s[20:21]
	v_mfma_f32_16x16x32_f16 v[26:29], v[88:91], v[144:147], v[26:29]
	v_mfma_f32_16x16x32_f16 v[22:25], v[96:99], v[144:147], v[22:25]
	v_mfma_f32_16x16x32_f16 v[42:45], v[92:95], v[140:143], v[42:45]
	v_mfma_f32_16x16x32_f16 v[38:41], v[100:103], v[140:143], v[38:41]
	v_mfma_f32_16x16x32_f16 v[26:29], v[92:95], v[148:151], v[26:29]
	v_mfma_f32_16x16x32_f16 v[22:25], v[100:103], v[148:151], v[22:25]
	v_mfma_f32_16x16x32_f16 v[78:81], v[104:107], v[120:123], v[78:81]
	v_mfma_f32_16x16x32_f16 v[74:77], v[112:115], v[120:123], v[74:77]
	v_mfma_f32_16x16x32_f16 v[66:69], v[104:107], v[128:131], v[66:69]
	v_mfma_f32_16x16x32_f16 v[62:65], v[112:115], v[128:131], v[62:65]
	v_mfma_f32_16x16x32_f16 v[78:81], v[108:111], v[124:127], v[78:81]
	v_mfma_f32_16x16x32_f16 v[74:77], v[116:119], v[124:127], v[74:77]
	v_mfma_f32_16x16x32_f16 v[66:69], v[108:111], v[132:135], v[66:69]
	v_mfma_f32_16x16x32_f16 v[62:65], v[116:119], v[132:135], v[62:65]
	v_mfma_f32_16x16x32_f16 v[50:53], v[104:107], v[136:139], v[50:53]
	v_mfma_f32_16x16x32_f16 v[46:49], v[112:115], v[136:139], v[46:49]
	s_add_i32 s7, s7, 1
	s_cmp_lg_u32 s7, 16
	v_mfma_f32_16x16x32_f16 v[34:37], v[104:107], v[144:147], v[34:37]
	s_cselect_b32 s7, s7, 0
	v_mfma_f32_16x16x32_f16 v[30:33], v[112:115], v[144:147], v[30:33]
	s_add_i32 s11, s11, -1
	v_mfma_f32_16x16x32_f16 v[50:53], v[108:111], v[140:143], v[50:53]
	s_mov_b32 s15, s13
	v_mfma_f32_16x16x32_f16 v[46:49], v[116:119], v[140:143], v[46:49]
	s_mov_b32 s13, s14
	v_mfma_f32_16x16x32_f16 v[34:37], v[108:111], v[148:151], v[34:37]
	s_mov_b32 s14, s16
	v_mfma_f32_16x16x32_f16 v[30:33], v[116:119], v[148:151], v[30:33]
	s_cmp_lg_u32 s11, 0
	s_setprio 0
	s_barrier
	s_cbranch_scc1 .LBB2_3
	v_lshl_add_u32 v0, s0, 7, v86
	v_or_b32_e32 v88, s10, v1
	v_ashrrev_i32_e32 v1, 31, v0
	v_lshlrev_b64 v[82:83], 12, v[0:1]
	v_or_b32_e32 v88, s1, v88
	v_lshl_add_u64 v[82:83], s[8:9], 0, v[82:83]
	v_lshlrev_b32_e32 v88, 2, v88
	v_mov_b32_e32 v89, 0
	v_or_b32_e32 v84, 16, v0
	v_lshl_add_u64 v[82:83], v[82:83], 0, v[88:89]
	v_pk_add_f32 v[20:21], v[16:17], v[20:21]
	v_pk_add_f32 v[18:19], v[14:15], v[18:19]
	v_ashrrev_i32_e32 v85, 31, v84
	global_store_dwordx4 v[82:83], v[18:21], off sc1
	v_lshlrev_b64 v[84:85], 12, v[84:85]
	v_lshl_add_u64 v[84:85], s[8:9], 0, v[84:85]
	v_pk_add_f32 v[20:21], v[12:13], v[72:73]
	v_pk_add_f32 v[18:19], v[10:11], v[70:71]
	global_store_dwordx4 v[82:83], v[18:21], off offset:64 sc1
	v_or_b32_e32 v86, 32, v0
	v_lshl_add_u64 v[84:85], v[84:85], 0, v[88:89]
	v_pk_add_f32 v[20:21], v[8:9], v[80:81]
	v_pk_add_f32 v[18:19], v[6:7], v[78:79]
	global_store_dwordx4 v[82:83], v[18:21], off offset:512 sc1
	v_ashrrev_i32_e32 v87, 31, v86
	v_lshlrev_b64 v[86:87], 12, v[86:87]
	v_pk_add_f32 v[20:21], v[4:5], v[76:77]
	v_pk_add_f32 v[18:19], v[2:3], v[74:75]
	global_store_dwordx4 v[82:83], v[18:21], off offset:576 sc1
	v_lshl_add_u64 v[86:87], s[8:9], 0, v[86:87]
	v_or_b32_e32 v0, 48, v0
	v_pk_add_f32 v[20:21], v[16:17], v[60:61]
	v_pk_add_f32 v[18:19], v[14:15], v[58:59]
	global_store_dwordx4 v[84:85], v[18:21], off sc1
	v_ashrrev_i32_e32 v1, 31, v0
	v_lshl_add_u64 v[86:87], v[86:87], 0, v[88:89]
	v_pk_add_f32 v[20:21], v[12:13], v[56:57]
	v_pk_add_f32 v[18:19], v[10:11], v[54:55]
	global_store_dwordx4 v[84:85], v[18:21], off offset:64 sc1
	v_lshlrev_b64 v[0:1], 12, v[0:1]
	v_lshl_add_u64 v[0:1], s[8:9], 0, v[0:1]
	v_pk_add_f32 v[20:21], v[8:9], v[68:69]
	v_pk_add_f32 v[18:19], v[6:7], v[66:67]
	global_store_dwordx4 v[84:85], v[18:21], off offset:512 sc1
	v_lshl_add_u64 v[0:1], v[0:1], 0, v[88:89]
	s_cmpk_gt_u32 s12, 0xff
	v_pk_add_f32 v[20:21], v[4:5], v[64:65]
	v_pk_add_f32 v[18:19], v[2:3], v[62:63]
	global_store_dwordx4 v[84:85], v[18:21], off offset:576 sc1
	s_nop 1
	v_pk_add_f32 v[20:21], v[16:17], v[44:45]
	v_pk_add_f32 v[18:19], v[14:15], v[42:43]
	global_store_dwordx4 v[86:87], v[18:21], off sc1
	v_pk_add_f32 v[16:17], v[16:17], v[28:29]
	v_pk_add_f32 v[14:15], v[14:15], v[26:27]
	v_pk_add_f32 v[20:21], v[12:13], v[40:41]
	v_pk_add_f32 v[18:19], v[10:11], v[38:39]
	global_store_dwordx4 v[86:87], v[18:21], off offset:64 sc1
	v_pk_add_f32 v[12:13], v[12:13], v[24:25]
	v_pk_add_f32 v[10:11], v[10:11], v[22:23]
	v_pk_add_f32 v[20:21], v[8:9], v[52:53]
	v_pk_add_f32 v[18:19], v[6:7], v[50:51]
	global_store_dwordx4 v[86:87], v[18:21], off offset:512 sc1
	v_pk_add_f32 v[8:9], v[8:9], v[36:37]
	v_pk_add_f32 v[6:7], v[6:7], v[34:35]
	v_pk_add_f32 v[20:21], v[4:5], v[48:49]
	v_pk_add_f32 v[18:19], v[2:3], v[46:47]
	v_pk_add_f32 v[4:5], v[4:5], v[32:33]
	v_pk_add_f32 v[2:3], v[2:3], v[30:31]
	global_store_dwordx4 v[86:87], v[18:21], off offset:576 sc1
	global_store_dwordx4 v[0:1], v[14:17], off sc1
	global_store_dwordx4 v[0:1], v[10:13], off offset:64 sc1
	global_store_dwordx4 v[0:1], v[6:9], off offset:512 sc1
	global_store_dwordx4 v[0:1], v[2:5], off offset:576 sc1
	s_waitcnt vmcnt(0)
	s_cbranch_scc1 .LBB2_6
	s_barrier
